# v8 + grid barrier: XCD leaders poll the TOP arrival counter directly instead of TOPGEN (one hop less)
# speedup vs baseline: 1.0338x; 1.0338x over previous
.LBB0_798:
	s_or_b64 exec, exec, s[8:9]
	s_waitcnt vmcnt(0)
	v_readfirstlane_b32 s6, v2
	v_cvt_f32_u32_e32 v2, v0
	v_sub_u32_e32 v3, 0, v0
	v_add_u32_e32 v1, s6, v1
	v_readlane_b32 s6, v254, 23
	v_rcp_iflag_f32_e32 v2, v2
	v_readlane_b32 s7, v254, 24
	s_mov_b64 s[8:9], -1
	v_mul_f32_e32 v2, 0x4f7ffffe, v2
	v_cvt_u32_f32_e32 v2, v2
	v_mul_lo_u32 v3, v3, v2
	v_mul_hi_u32 v3, v2, v3
	v_add_u32_e32 v2, v2, v3
	v_mul_hi_u32 v2, v1, v2
	v_mul_lo_u32 v3, v2, v0
	v_sub_u32_e32 v3, v1, v3
	v_cmp_ge_u32_e32 vcc, v3, v0
	v_add_u32_e32 v4, 1, v2
	v_add_u32_e32 v1, 1, v1
	v_cndmask_b32_e32 v2, v2, v4, vcc
	v_sub_u32_e32 v4, v3, v0
	v_cndmask_b32_e32 v3, v3, v4, vcc
	v_cmp_ge_u32_e32 vcc, v3, v0
	v_add_u32_e32 v3, 1, v2
	s_nop 0
	v_cndmask_b32_e32 v2, v2, v3, vcc
	v_mul_lo_u32 v3, v0, v2
	v_add_u32_e32 v0, v3, v0
	v_cmp_ne_u32_e32 vcc, v1, v0
	v_mov_b32_e32 v4, v0
	v_mov_b64_e32 v[0:1], s[6:7]
	s_and_saveexec_b64 s[6:7], vcc
	s_cbranch_execz .LBB0_810
	v_readlane_b32 s8, v254, 21
	v_readlane_b32 s9, v254, 22
	s_mov_b64 s[10:11], 0
	s_nop 3
	global_load_dword v0, v65, s[8:9] sc1
	s_waitcnt vmcnt(0)
	v_sub_u32_e32 v0, v0, v4
	v_cmp_gt_i32_e32 vcc, 0, v0
	s_and_saveexec_b64 s[8:9], vcc
	s_cbranch_execz .LBB0_809
	s_mov_b32 s21, 1
	s_branch .LBB0_802

.LBB0_804:
	v_readlane_b32 s14, v254, 21
	v_readlane_b32 s15, v254, 22
	s_add_i32 s21, s21, 1
	s_mov_b64 s[16:17], -1
	s_nop 2
	global_load_dword v0, v65, s[14:15] sc1
	s_waitcnt vmcnt(0)
	v_sub_u32_e32 v0, v0, v4
	v_cmp_le_i32_e32 vcc, 0, v0
	s_orn2_b64 s[14:15], vcc, exec
	s_branch .LBB0_801

.LBB0_2535:
	s_or_b64 exec, exec, s[8:9]
	s_waitcnt vmcnt(0)
	v_readfirstlane_b32 s6, v2
	v_cvt_f32_u32_e32 v2, v0
	v_sub_u32_e32 v3, 0, v0
	v_add_u32_e32 v1, s6, v1
	v_readlane_b32 s6, v254, 23
	v_rcp_iflag_f32_e32 v2, v2
	v_readlane_b32 s7, v254, 24
	s_mov_b64 s[8:9], -1
	v_mul_f32_e32 v2, 0x4f7ffffe, v2
	v_cvt_u32_f32_e32 v2, v2
	v_mul_lo_u32 v3, v3, v2
	v_mul_hi_u32 v3, v2, v3
	v_add_u32_e32 v2, v2, v3
	v_mul_hi_u32 v2, v1, v2
	v_mul_lo_u32 v3, v2, v0
	v_sub_u32_e32 v3, v1, v3
	v_cmp_ge_u32_e32 vcc, v3, v0
	v_add_u32_e32 v4, 1, v2
	v_add_u32_e32 v1, 1, v1
	v_cndmask_b32_e32 v2, v2, v4, vcc
	v_sub_u32_e32 v4, v3, v0
	v_cndmask_b32_e32 v3, v3, v4, vcc
	v_cmp_ge_u32_e32 vcc, v3, v0
	v_add_u32_e32 v3, 1, v2
	s_nop 0
	v_cndmask_b32_e32 v2, v2, v3, vcc
	v_mul_lo_u32 v3, v0, v2
	v_add_u32_e32 v0, v3, v0
	v_cmp_ne_u32_e32 vcc, v1, v0
	v_mov_b32_e32 v4, v0
	v_mov_b64_e32 v[0:1], s[6:7]
	s_and_saveexec_b64 s[6:7], vcc
	s_cbranch_execz .LBB0_2547
	v_readlane_b32 s8, v254, 21
	v_readlane_b32 s9, v254, 22
	s_mov_b64 s[10:11], 0
	s_nop 3
	global_load_dword v0, v65, s[8:9] sc1
	s_waitcnt vmcnt(0)
	v_sub_u32_e32 v0, v0, v4
	v_cmp_gt_i32_e32 vcc, 0, v0
	s_and_saveexec_b64 s[8:9], vcc
	s_cbranch_execz .LBB0_2546
	s_mov_b32 s20, 1
	s_branch .LBB0_2539

.LBB0_2541:
	v_readlane_b32 s14, v254, 21
	v_readlane_b32 s15, v254, 22
	s_add_i32 s20, s20, 1
	s_mov_b64 s[16:17], -1
	s_nop 2
	global_load_dword v0, v65, s[14:15] sc1
	s_waitcnt vmcnt(0)
	v_sub_u32_e32 v0, v0, v4
	v_cmp_le_i32_e32 vcc, 0, v0
	s_orn2_b64 s[14:15], vcc, exec
	s_branch .LBB0_2538
